# prologue modulation GEMV: the 34 serial load-wait-silu-store iterations that fill the LDS image of silu(c) become two batches of 17 loads in flight
# speedup vs baseline: 1.0211x; 1.0079x over previous
.LBB0_13:
	s_mov_b32 s79, 0
.Lmy_fill:
	v_add_u32_e32 v76, 0, v70
	v_add_u32_e32 v77, 0, v5
	v_and_b32_e32 v71, 0x7800, v77
	v_cmp_gt_u32_e32 vcc, s40, v76
	v_and_b32_e32 v2, 0x3ff, v76
	v_mov_b32_e32 v72, s25
	v_mov_b32_e32 v73, s1
	v_mov_b32_e32 v74, s24
	v_mov_b32_e32 v75, s0
	v_cndmask_b32_e32 v71, 0, v71, vcc
	v_cndmask_b32_e32 v73, v72, v73, vcc
	v_cndmask_b32_e32 v72, v74, v75, vcc
	v_or3_b32 v2, v2, v71, s31
	v_lshl_add_u64 v[72:73], v[2:3], 2, v[72:73]
	global_load_dword v94, v[72:73], off
	v_add_u32_e32 v76, 512, v70
	v_add_u32_e32 v77, 1024, v5
	v_and_b32_e32 v71, 0x7800, v77
	v_cmp_gt_u32_e32 vcc, s40, v76
	v_and_b32_e32 v2, 0x3ff, v76
	v_mov_b32_e32 v72, s25
	v_mov_b32_e32 v73, s1
	v_mov_b32_e32 v74, s24
	v_mov_b32_e32 v75, s0
	v_cndmask_b32_e32 v71, 0, v71, vcc
	v_cndmask_b32_e32 v73, v72, v73, vcc
	v_cndmask_b32_e32 v72, v74, v75, vcc
	v_or3_b32 v2, v2, v71, s31
	v_lshl_add_u64 v[72:73], v[2:3], 2, v[72:73]
	global_load_dword v95, v[72:73], off
	v_add_u32_e32 v76, 1024, v70
	v_add_u32_e32 v77, 2048, v5
	v_and_b32_e32 v71, 0x7800, v77
	v_cmp_gt_u32_e32 vcc, s40, v76
	v_and_b32_e32 v2, 0x3ff, v76
	v_mov_b32_e32 v72, s25
	v_mov_b32_e32 v73, s1
	v_mov_b32_e32 v74, s24
	v_mov_b32_e32 v75, s0
	v_cndmask_b32_e32 v71, 0, v71, vcc
	v_cndmask_b32_e32 v73, v72, v73, vcc
	v_cndmask_b32_e32 v72, v74, v75, vcc
	v_or3_b32 v2, v2, v71, s31
	v_lshl_add_u64 v[72:73], v[2:3], 2, v[72:73]
	global_load_dword v96, v[72:73], off
	v_add_u32_e32 v76, 1536, v70
	v_add_u32_e32 v77, 3072, v5
	v_and_b32_e32 v71, 0x7800, v77
	v_cmp_gt_u32_e32 vcc, s40, v76
	v_and_b32_e32 v2, 0x3ff, v76
	v_mov_b32_e32 v72, s25
	v_mov_b32_e32 v73, s1
	v_mov_b32_e32 v74, s24
	v_mov_b32_e32 v75, s0
	v_cndmask_b32_e32 v71, 0, v71, vcc
	v_cndmask_b32_e32 v73, v72, v73, vcc
	v_cndmask_b32_e32 v72, v74, v75, vcc
	v_or3_b32 v2, v2, v71, s31
	v_lshl_add_u64 v[72:73], v[2:3], 2, v[72:73]
	global_load_dword v97, v[72:73], off
	v_add_u32_e32 v76, 2048, v70
	v_add_u32_e32 v77, 4096, v5
	v_and_b32_e32 v71, 0x7800, v77
	v_cmp_gt_u32_e32 vcc, s40, v76
	v_and_b32_e32 v2, 0x3ff, v76
	v_mov_b32_e32 v72, s25
	v_mov_b32_e32 v73, s1
	v_mov_b32_e32 v74, s24
	v_mov_b32_e32 v75, s0
	v_cndmask_b32_e32 v71, 0, v71, vcc
	v_cndmask_b32_e32 v73, v72, v73, vcc
	v_cndmask_b32_e32 v72, v74, v75, vcc
	v_or3_b32 v2, v2, v71, s31
	v_lshl_add_u64 v[72:73], v[2:3], 2, v[72:73]
	global_load_dword v98, v[72:73], off
	v_add_u32_e32 v76, 2560, v70
	v_add_u32_e32 v77, 5120, v5
	v_and_b32_e32 v71, 0x7800, v77
	v_cmp_gt_u32_e32 vcc, s40, v76
	v_and_b32_e32 v2, 0x3ff, v76
	v_mov_b32_e32 v72, s25
	v_mov_b32_e32 v73, s1
	v_mov_b32_e32 v74, s24
	v_mov_b32_e32 v75, s0
	v_cndmask_b32_e32 v71, 0, v71, vcc
	v_cndmask_b32_e32 v73, v72, v73, vcc
	v_cndmask_b32_e32 v72, v74, v75, vcc
	v_or3_b32 v2, v2, v71, s31
	v_lshl_add_u64 v[72:73], v[2:3], 2, v[72:73]
	global_load_dword v99, v[72:73], off
	v_add_u32_e32 v76, 3072, v70
	v_add_u32_e32 v77, 6144, v5
	v_and_b32_e32 v71, 0x7800, v77
	v_cmp_gt_u32_e32 vcc, s40, v76
	v_and_b32_e32 v2, 0x3ff, v76
	v_mov_b32_e32 v72, s25
	v_mov_b32_e32 v73, s1
	v_mov_b32_e32 v74, s24
	v_mov_b32_e32 v75, s0
	v_cndmask_b32_e32 v71, 0, v71, vcc
	v_cndmask_b32_e32 v73, v72, v73, vcc
	v_cndmask_b32_e32 v72, v74, v75, vcc
	v_or3_b32 v2, v2, v71, s31
	v_lshl_add_u64 v[72:73], v[2:3], 2, v[72:73]
	global_load_dword v100, v[72:73], off
	v_add_u32_e32 v76, 3584, v70
	v_add_u32_e32 v77, 7168, v5
	v_and_b32_e32 v71, 0x7800, v77
	v_cmp_gt_u32_e32 vcc, s40, v76
	v_and_b32_e32 v2, 0x3ff, v76
	v_mov_b32_e32 v72, s25
	v_mov_b32_e32 v73, s1
	v_mov_b32_e32 v74, s24
	v_mov_b32_e32 v75, s0
	v_cndmask_b32_e32 v71, 0, v71, vcc
	v_cndmask_b32_e32 v73, v72, v73, vcc
	v_cndmask_b32_e32 v72, v74, v75, vcc
	v_or3_b32 v2, v2, v71, s31
	v_lshl_add_u64 v[72:73], v[2:3], 2, v[72:73]
	global_load_dword v101, v[72:73], off
	v_add_u32_e32 v76, 4096, v70
	v_add_u32_e32 v77, 8192, v5
	v_and_b32_e32 v71, 0x7800, v77
	v_cmp_gt_u32_e32 vcc, s40, v76
	v_and_b32_e32 v2, 0x3ff, v76
	v_mov_b32_e32 v72, s25
	v_mov_b32_e32 v73, s1
	v_mov_b32_e32 v74, s24
	v_mov_b32_e32 v75, s0
	v_cndmask_b32_e32 v71, 0, v71, vcc
	v_cndmask_b32_e32 v73, v72, v73, vcc
	v_cndmask_b32_e32 v72, v74, v75, vcc
	v_or3_b32 v2, v2, v71, s31
	v_lshl_add_u64 v[72:73], v[2:3], 2, v[72:73]
	global_load_dword v102, v[72:73], off
	v_add_u32_e32 v76, 4608, v70
	v_add_u32_e32 v77, 9216, v5
	v_and_b32_e32 v71, 0x7800, v77
	v_cmp_gt_u32_e32 vcc, s40, v76
	v_and_b32_e32 v2, 0x3ff, v76
	v_mov_b32_e32 v72, s25
	v_mov_b32_e32 v73, s1
	v_mov_b32_e32 v74, s24
	v_mov_b32_e32 v75, s0
	v_cndmask_b32_e32 v71, 0, v71, vcc
	v_cndmask_b32_e32 v73, v72, v73, vcc
	v_cndmask_b32_e32 v72, v74, v75, vcc
	v_or3_b32 v2, v2, v71, s31
	v_lshl_add_u64 v[72:73], v[2:3], 2, v[72:73]
	global_load_dword v103, v[72:73], off
	v_add_u32_e32 v76, 5120, v70
	v_add_u32_e32 v77, 10240, v5
	v_and_b32_e32 v71, 0x7800, v77
	v_cmp_gt_u32_e32 vcc, s40, v76
	v_and_b32_e32 v2, 0x3ff, v76
	v_mov_b32_e32 v72, s25
	v_mov_b32_e32 v73, s1
	v_mov_b32_e32 v74, s24
	v_mov_b32_e32 v75, s0
	v_cndmask_b32_e32 v71, 0, v71, vcc
	v_cndmask_b32_e32 v73, v72, v73, vcc
	v_cndmask_b32_e32 v72, v74, v75, vcc
	v_or3_b32 v2, v2, v71, s31
	v_lshl_add_u64 v[72:73], v[2:3], 2, v[72:73]
	global_load_dword v104, v[72:73], off
	v_add_u32_e32 v76, 5632, v70
	v_add_u32_e32 v77, 11264, v5
	v_and_b32_e32 v71, 0x7800, v77
	v_cmp_gt_u32_e32 vcc, s40, v76
	v_and_b32_e32 v2, 0x3ff, v76
	v_mov_b32_e32 v72, s25
	v_mov_b32_e32 v73, s1
	v_mov_b32_e32 v74, s24
	v_mov_b32_e32 v75, s0
	v_cndmask_b32_e32 v71, 0, v71, vcc
	v_cndmask_b32_e32 v73, v72, v73, vcc
	v_cndmask_b32_e32 v72, v74, v75, vcc
	v_or3_b32 v2, v2, v71, s31
	v_lshl_add_u64 v[72:73], v[2:3], 2, v[72:73]
	global_load_dword v105, v[72:73], off
	v_add_u32_e32 v76, 6144, v70
	v_add_u32_e32 v77, 12288, v5
	v_and_b32_e32 v71, 0x7800, v77
	v_cmp_gt_u32_e32 vcc, s40, v76
	v_and_b32_e32 v2, 0x3ff, v76
	v_mov_b32_e32 v72, s25
	v_mov_b32_e32 v73, s1
	v_mov_b32_e32 v74, s24
	v_mov_b32_e32 v75, s0
	v_cndmask_b32_e32 v71, 0, v71, vcc
	v_cndmask_b32_e32 v73, v72, v73, vcc
	v_cndmask_b32_e32 v72, v74, v75, vcc
	v_or3_b32 v2, v2, v71, s31
	v_lshl_add_u64 v[72:73], v[2:3], 2, v[72:73]
	global_load_dword v106, v[72:73], off
	v_add_u32_e32 v76, 6656, v70
	v_add_u32_e32 v77, 13312, v5
	v_and_b32_e32 v71, 0x7800, v77
	v_cmp_gt_u32_e32 vcc, s40, v76
	v_and_b32_e32 v2, 0x3ff, v76
	v_mov_b32_e32 v72, s25
	v_mov_b32_e32 v73, s1
	v_mov_b32_e32 v74, s24
	v_mov_b32_e32 v75, s0
	v_cndmask_b32_e32 v71, 0, v71, vcc
	v_cndmask_b32_e32 v73, v72, v73, vcc
	v_cndmask_b32_e32 v72, v74, v75, vcc
	v_or3_b32 v2, v2, v71, s31
	v_lshl_add_u64 v[72:73], v[2:3], 2, v[72:73]
	global_load_dword v107, v[72:73], off
	v_add_u32_e32 v76, 7168, v70
	v_add_u32_e32 v77, 14336, v5
	v_and_b32_e32 v71, 0x7800, v77
	v_cmp_gt_u32_e32 vcc, s40, v76
	v_and_b32_e32 v2, 0x3ff, v76
	v_mov_b32_e32 v72, s25
	v_mov_b32_e32 v73, s1
	v_mov_b32_e32 v74, s24
	v_mov_b32_e32 v75, s0
	v_cndmask_b32_e32 v71, 0, v71, vcc
	v_cndmask_b32_e32 v73, v72, v73, vcc
	v_cndmask_b32_e32 v72, v74, v75, vcc
	v_or3_b32 v2, v2, v71, s31
	v_lshl_add_u64 v[72:73], v[2:3], 2, v[72:73]
	global_load_dword v108, v[72:73], off
	v_add_u32_e32 v76, 7680, v70
	v_add_u32_e32 v77, 15360, v5
	v_and_b32_e32 v71, 0x7800, v77
	v_cmp_gt_u32_e32 vcc, s40, v76
	v_and_b32_e32 v2, 0x3ff, v76
	v_mov_b32_e32 v72, s25
	v_mov_b32_e32 v73, s1
	v_mov_b32_e32 v74, s24
	v_mov_b32_e32 v75, s0
	v_cndmask_b32_e32 v71, 0, v71, vcc
	v_cndmask_b32_e32 v73, v72, v73, vcc
	v_cndmask_b32_e32 v72, v74, v75, vcc
	v_or3_b32 v2, v2, v71, s31
	v_lshl_add_u64 v[72:73], v[2:3], 2, v[72:73]
	global_load_dword v109, v[72:73], off
	v_add_u32_e32 v76, 8192, v70
	v_add_u32_e32 v77, 16384, v5
	v_and_b32_e32 v71, 0x7800, v77
	v_cmp_gt_u32_e32 vcc, s40, v76
	v_and_b32_e32 v2, 0x3ff, v76
	v_mov_b32_e32 v72, s25
	v_mov_b32_e32 v73, s1
	v_mov_b32_e32 v74, s24
	v_mov_b32_e32 v75, s0
	v_cndmask_b32_e32 v71, 0, v71, vcc
	v_cndmask_b32_e32 v73, v72, v73, vcc
	v_cndmask_b32_e32 v72, v74, v75, vcc
	v_or3_b32 v2, v2, v71, s31
	v_lshl_add_u64 v[72:73], v[2:3], 2, v[72:73]
	global_load_dword v110, v[72:73], off
	s_waitcnt vmcnt(0)
	v_mul_f32_e32 v72, 0xbfb8aa3b, v94
	v_exp_f32_e32 v72, v72
	s_nop 0
	v_add_f32_e32 v73, 1.0, v72
	v_rcp_f32_e32 v72, v73
	s_nop 0
	v_mul_f32_e32 v2, v94, v72
	ds_write_b32 v4, v2 offset:0
	v_mul_f32_e32 v72, 0xbfb8aa3b, v95
	v_exp_f32_e32 v72, v72
	s_nop 0
	v_add_f32_e32 v73, 1.0, v72
	v_rcp_f32_e32 v72, v73
	s_nop 0
	v_mul_f32_e32 v2, v95, v72
	ds_write_b32 v4, v2 offset:2048
	v_mul_f32_e32 v72, 0xbfb8aa3b, v96
	v_exp_f32_e32 v72, v72
	s_nop 0
	v_add_f32_e32 v73, 1.0, v72
	v_rcp_f32_e32 v72, v73
	s_nop 0
	v_mul_f32_e32 v2, v96, v72
	ds_write_b32 v4, v2 offset:4096
	v_mul_f32_e32 v72, 0xbfb8aa3b, v97
	v_exp_f32_e32 v72, v72
	s_nop 0
	v_add_f32_e32 v73, 1.0, v72
	v_rcp_f32_e32 v72, v73
	s_nop 0
	v_mul_f32_e32 v2, v97, v72
	ds_write_b32 v4, v2 offset:6144
	v_mul_f32_e32 v72, 0xbfb8aa3b, v98
	v_exp_f32_e32 v72, v72
	s_nop 0
	v_add_f32_e32 v73, 1.0, v72
	v_rcp_f32_e32 v72, v73
	s_nop 0
	v_mul_f32_e32 v2, v98, v72
	ds_write_b32 v4, v2 offset:8192
	v_mul_f32_e32 v72, 0xbfb8aa3b, v99
	v_exp_f32_e32 v72, v72
	s_nop 0
	v_add_f32_e32 v73, 1.0, v72
	v_rcp_f32_e32 v72, v73
	s_nop 0
	v_mul_f32_e32 v2, v99, v72
	ds_write_b32 v4, v2 offset:10240
	v_mul_f32_e32 v72, 0xbfb8aa3b, v100
	v_exp_f32_e32 v72, v72
	s_nop 0
	v_add_f32_e32 v73, 1.0, v72
	v_rcp_f32_e32 v72, v73
	s_nop 0
	v_mul_f32_e32 v2, v100, v72
	ds_write_b32 v4, v2 offset:12288
	v_mul_f32_e32 v72, 0xbfb8aa3b, v101
	v_exp_f32_e32 v72, v72
	s_nop 0
	v_add_f32_e32 v73, 1.0, v72
	v_rcp_f32_e32 v72, v73
	s_nop 0
	v_mul_f32_e32 v2, v101, v72
	ds_write_b32 v4, v2 offset:14336
	v_mul_f32_e32 v72, 0xbfb8aa3b, v102
	v_exp_f32_e32 v72, v72
	s_nop 0
	v_add_f32_e32 v73, 1.0, v72
	v_rcp_f32_e32 v72, v73
	s_nop 0
	v_mul_f32_e32 v2, v102, v72
	ds_write_b32 v4, v2 offset:16384
	v_mul_f32_e32 v72, 0xbfb8aa3b, v103
	v_exp_f32_e32 v72, v72
	s_nop 0
	v_add_f32_e32 v73, 1.0, v72
	v_rcp_f32_e32 v72, v73
	s_nop 0
	v_mul_f32_e32 v2, v103, v72
	ds_write_b32 v4, v2 offset:18432
	v_mul_f32_e32 v72, 0xbfb8aa3b, v104
	v_exp_f32_e32 v72, v72
	s_nop 0
	v_add_f32_e32 v73, 1.0, v72
	v_rcp_f32_e32 v72, v73
	s_nop 0
	v_mul_f32_e32 v2, v104, v72
	ds_write_b32 v4, v2 offset:20480
	v_mul_f32_e32 v72, 0xbfb8aa3b, v105
	v_exp_f32_e32 v72, v72
	s_nop 0
	v_add_f32_e32 v73, 1.0, v72
	v_rcp_f32_e32 v72, v73
	s_nop 0
	v_mul_f32_e32 v2, v105, v72
	ds_write_b32 v4, v2 offset:22528
	v_mul_f32_e32 v72, 0xbfb8aa3b, v106
	v_exp_f32_e32 v72, v72
	s_nop 0
	v_add_f32_e32 v73, 1.0, v72
	v_rcp_f32_e32 v72, v73
	s_nop 0
	v_mul_f32_e32 v2, v106, v72
	ds_write_b32 v4, v2 offset:24576
	v_mul_f32_e32 v72, 0xbfb8aa3b, v107
	v_exp_f32_e32 v72, v72
	s_nop 0
	v_add_f32_e32 v73, 1.0, v72
	v_rcp_f32_e32 v72, v73
	s_nop 0
	v_mul_f32_e32 v2, v107, v72
	ds_write_b32 v4, v2 offset:26624
	v_mul_f32_e32 v72, 0xbfb8aa3b, v108
	v_exp_f32_e32 v72, v72
	s_nop 0
	v_add_f32_e32 v73, 1.0, v72
	v_rcp_f32_e32 v72, v73
	s_nop 0
	v_mul_f32_e32 v2, v108, v72
	ds_write_b32 v4, v2 offset:28672
	v_mul_f32_e32 v72, 0xbfb8aa3b, v109
	v_exp_f32_e32 v72, v72
	s_nop 0
	v_add_f32_e32 v73, 1.0, v72
	v_rcp_f32_e32 v72, v73
	s_nop 0
	v_mul_f32_e32 v2, v109, v72
	ds_write_b32 v4, v2 offset:30720
	v_mul_f32_e32 v72, 0xbfb8aa3b, v110
	v_exp_f32_e32 v72, v72
	s_nop 0
	v_add_f32_e32 v73, 1.0, v72
	v_rcp_f32_e32 v72, v73
	s_nop 0
	v_mul_f32_e32 v2, v110, v72
	ds_write_b32 v4, v2 offset:32768
	v_add_u32_e32 v70, 0x2200, v70
	v_add_u32_e32 v5, 0x4400, v5
	v_add_u32_e32 v4, 0x8800, v4
	s_add_i32 s79, s79, 1
	s_cmp_lt_u32 s79, 2
	s_cbranch_scc1 .Lmy_fill
	s_or_b64 exec, exec, s[36:37]
	v_add_u32_e32 v2, s31, v164
	v_mad_i64_i32 v[4:5], s[36:37], v2, s39, v[158:159]
	s_mov_b32 s31, -16
	v_mov_b32_e32 v2, v168
	s_waitcnt lgkmcnt(0)
	s_barrier
